# exact lgkmcnt waits in attention halves + static prio for waves 4-7 in attention + combine loop: row loads issued before the blocking slot-index fetch
# speedup vs baseline: 1.0086x; 1.0086x over previous
; DEVI int tidx() { int t = threadIdx.x; asm volatile("" : "+v"(t)); __builtin_assume(t >= 0 && t < 512); return t; }
; DEVI int bidx() { int b = blockIdx.x; asm volatile("" : "+s"(b)); __builtin_assume(b >= 0 && b < 65536); return b; }
; DEVI void attn_unit8(const Params& p, char* smem, int unit, int l, int& cvs  , CvRun& crun) {
;     const int tid = tidx(), wid = __builtin_amdgcn_readfirstlane(tid >> 6), lane = tid & 63, r32 = lane & 31, hi = lane >> 5;
;     const int x8 = unit & 7, v8 = unit >> 3, bh = x8 + 8 * (v8 >> 4), qt = v8 & 15, b = bh >> 3, hh = bh & 7;
;     char* K_lds = smem; char* V_lds = smem + 73728;
;     float* wsx = (float*)(smem + 122880) + wid * 64; float* li_l = wsx; float* al_l = wsx + 32;
;     const bf16_t* Kg = p.kfull + (size_t)bh * S_ * 96; const bf16_t* Vg = p.vfull + (size_t)bh * S_ * 64;
;     const size_t qtok = (size_t)b * S_ + qt * 256 + wid * 32 + r32;
; DEVI void phase_attn(const Params& p, char* smem, int l) {
;     mlstm_scan(p);
;     const int lane = tidx() & 63, wid = __builtin_amdgcn_readfirstlane(tidx() >> 6);
;     int cvs = bidx() * 8 + wid;
;     CvRun crun; crun.left = 0; crun.sstep = 0; crun.dstep = 0;
;     for (int u = bidx(); u < 64 * 16; u += gridDim.x) attn_unit8(p, smem, u, l, cvs, crun);
.LBB0_662:
	s_or_b64 exec, exec, s[16:17]
	v_mov_b32_e32 v1, v0
	v_mov_b32_e32 v2, v0
	s_mov_b32 s62, s84
	v_readfirstlane_b32 s2, v2
	s_lshr_b32 s4, s2, 6
	s_mov_b32 s2, s84
	s_lshl_b32 s2, s2, 3
	s_add_i32 s54, s2, s4
	v_writelane_b32 v248, s4, 6
	s_cmpk_gt_u32 s62, 0x3ff
	v_writelane_b32 v248, s84, 7
	s_cbranch_scc1 .LBB0_778
	v_readlane_b32 s98, v248, 6
	s_nop 3
	s_cmp_lt_u32 s98, 4
	s_cbranch_scc1 .Lmy_prio_a
	s_setprio 1
.Lmy_prio_a:
	s_and_b32 s2, s33, 63
	s_cmp_eq_u32 s2, 0
	s_cselect_b64 s[30:31], -1, 0
	s_ashr_i32 s4, s33, 5
	s_abs_i32 s63, s4
	v_cvt_f32_u32_e32 v2, s63
	s_ashr_i32 s5, s4, 31
	s_lshl_b64 s[34:35], s[4:5], 18
	s_ashr_i32 s4, s33, 6
	v_rcp_iflag_f32_e32 v2, v2
	s_abs_i32 s64, s4
	v_cvt_f32_u32_e32 v3, s64
	s_ashr_i32 s5, s4, 31
	v_mul_f32_e32 v2, 0x4f7ffffe, v2
	v_cvt_u32_f32_e32 v2, v2
	v_rcp_iflag_f32_e32 v3, v3
	s_lshl_b64 s[36:37], s[4:5], 18
	s_lshl_b64 s[38:39], s[4:5], 19
	v_readfirstlane_b32 s4, v2
	v_mul_f32_e32 v2, 0x4f7ffffe, v3
	v_cvt_u32_f32_e32 v2, v2
	s_sub_i32 s2, 0, s63
	s_mul_i32 s2, s2, s4
	s_mul_hi_u32 s2, s4, s2
	s_add_i32 s65, s4, s2
	s_sub_i32 s2, 0, s64
	v_readfirstlane_b32 s4, v2
	s_mul_i32 s2, s2, s4
	s_mul_hi_u32 s2, s4, s2
	s_mov_b32 s9, 0
	s_add_i32 s66, s4, s2
	s_lshl_b32 s67, s33, 13
	s_lshl_b32 s68, s33, 8
	s_lshl_b32 s69, s33, 7
	s_lshl_b32 s72, s33, 6
	s_lshl_b32 s73, s33, 4
	s_mov_b64 s[26:27], 0
	v_mov_b32_e32 v175, 0
	v_mov_b32_e32 v177, 0x600
	s_mov_b32 s74, 0xaaab
	s_add_i32 s75, 0, 0x12000
	s_mov_b64 s[40:41], 0x2000
	s_mov_b64 s[42:43], 0x6000
	s_mov_b64 s[44:45], 0x4000
	s_movk_i32 s76, 0x80
	s_movk_i32 s77, 0x44
	s_mov_b64 s[46:47], 0x8000
	s_movk_i32 s78, 0xd8
	s_mov_b32 s79, 0x41000000
	s_add_i32 s80, 0, 0x14000
	s_add_i32 s81, 0, 0x16000
	s_add_i32 s82, 0, 0x18000
	v_mov_b32_e32 v181, 0x41800000
	s_mov_b32 s83, s62
	s_mov_b64 s[28:29], 0
	s_mov_b32 s56, 0
	s_branch .LBB0_665

; template <bool FIRST> DEVI bool partialSM(f32x16& p0, f32x16& p1, float& m_reg, float& alpha) {
;     float pmax = p0[0];
; #pragma unroll
;     for (int r = 1; r < 16; ++r) pmax = fmaxf(pmax, p0[r]);
; #pragma unroll
;     for (int r = 0; r < 16; ++r) pmax = fmaxf(pmax, p1[r]);
;     { auto rr = __builtin_amdgcn_permlane32_swap(__float_as_uint(pmax), __float_as_uint(pmax), false, false);
;       pmax = fmaxf(__uint_as_float(rr[0]), __uint_as_float(rr[1])); }
;     if (FIRST) { m_reg = pmax; alpha = 1.f;
; #pragma unroll
;         for (int r = 0; r < 16; ++r) { p0[r] = __builtin_amdgcn_exp2f(p0[r] - pmax); p1[r] = p1[r] - pmax; }
;         return false;
;     } else if (__builtin_expect(__all(pmax <= ATT_THR), 1)) { alpha = 1.f;
; #pragma unroll
;         for (int r = 0; r < 16; ++r) p0[r] = __builtin_amdgcn_exp2f(p0[r]);
;         return false;
;     } else { const float d = fmaxf(pmax, 0.f); alpha = __builtin_amdgcn_exp2f(-d); m_reg += d;
; #pragma unroll
;         for (int r = 0; r < 16; ++r) { p0[r] = __builtin_amdgcn_exp2f(p0[r] - d); p1[r] = p1[r] - d; }
;         return true;
;     }
; }
; DEVI void finishSM(f32x16& p0, f32x16& p1, float alpha, float& l_reg, bf16x8& pa0, bf16x8& pa1, bf16x8& pa2, bf16x8& pa3) {
; #pragma unroll
;     for (int r = 0; r < 16; ++r) p1[r] = __builtin_amdgcn_exp2f(p1[r]);
;     f32x2 s2 = (f32x2){p0[0], p0[1]} + (f32x2){p1[0], p1[1]};
; #pragma unroll
;     for (int r = 2; r < 16; r += 2) s2 += (f32x2){p0[r], p0[r + 1]} + (f32x2){p1[r], p1[r + 1]};
;     float ps = s2[0] + s2[1];
;     { auto rr = __builtin_amdgcn_permlane32_swap(__float_as_uint(ps), __float_as_uint(ps), false, false);
;       ps = __uint_as_float(rr[0]) + __uint_as_float(rr[1]); }
;     l_reg = l_reg * alpha + ps;
;     ...
;     PK4(p0, 0, pa0); PK4(p0, 8, pa1); PK4(p1, 0, pa2); PK4(p1, 8, pa3);
;     ...
; }
; DEVI void qkt(f32x16& p0, f32x16& p1, const char* Kb, const bf16x8 (&qr)[6], int r32, int hi, const f32x16& cinit) {
; #pragma unroll
;     for (int d0 = 0; d0 < 6; ++d0) { const int cb = (d0 * 16 + hi * 8) * 2;
;         const bf16x8 k0 = *(const bf16x8*)(Kb + KSWZ(r32, cb)), k1 = *(const bf16x8*)(Kb + KSWZ(32 + r32, cb));
;         p0 = __builtin_amdgcn_mfma_f32_32x32x16_bf16(k0, qr[d0], d0 == 0 ? cinit : p0, 0, 0, 0);
;         p1 = __builtin_amdgcn_mfma_f32_32x32x16_bf16(k1, qr[d0], d0 == 0 ? cinit : p1, 0, 0, 0); }
; }
.LBB0_696:
	s_mul_i32 s6, s89, 0x6000
	s_add_i32 s6, s6, 0
	v_add_u32_e32 v86, s6, v129
	ds_read_b128 v[82:85], v86 offset:12288
	ds_read_b128 v[124:127], v86 offset:18432
	v_add_u32_e32 v174, s6, v204
	v_exp_f32_e32 v66, v66
	v_exp_f32_e32 v67, v67
	s_waitcnt lgkmcnt(1)
	v_mfma_f32_32x32x16_bf16 v[98:113], v[82:85], v[150:153], v[34:49]
	v_add_u32_e32 v82, s6, v184
	v_add_u32_e32 v83, s6, v185
	ds_read_b128 v[208:211], v82 offset:12288
	ds_read_b128 v[212:215], v82 offset:18432
	ds_read_b128 v[216:219], v83 offset:12288
	ds_read_b128 v[220:223], v83 offset:18432
	v_exp_f32_e32 v68, v68
	v_exp_f32_e32 v69, v69
	v_exp_f32_e32 v70, v70
	v_exp_f32_e32 v71, v71
	s_waitcnt lgkmcnt(4)
	v_mfma_f32_32x32x16_bf16 v[82:97], v[124:127], v[150:153], v[34:49]
	ds_read_b128 v[124:127], v174 offset:12288
	ds_read_b128 v[224:227], v174 offset:18432
	v_exp_f32_e32 v72, v72
	v_exp_f32_e32 v73, v73
	v_exp_f32_e32 v74, v74
	v_exp_f32_e32 v75, v75
	v_exp_f32_e32 v76, v76
	v_exp_f32_e32 v77, v77
	s_waitcnt lgkmcnt(5)
	v_mfma_f32_32x32x16_bf16 v[98:113], v[208:211], v[138:141], v[98:113]
	v_add_u32_e32 v174, s6, v205
	v_exp_f32_e32 v78, v78
	v_exp_f32_e32 v79, v79
	ds_read_b128 v[228:231], v174 offset:12288
	ds_read_b128 v[232:235], v174 offset:18432
	v_exp_f32_e32 v80, v80
	v_exp_f32_e32 v81, v81
	v_add_u32_e32 v174, s6, v206
	s_waitcnt lgkmcnt(6)
	v_mfma_f32_32x32x16_bf16 v[82:97], v[212:215], v[138:141], v[82:97]
	v_add_f32_e64 v212, v50, v66
	v_add_f32_e64 v213, v51, v67
	v_add_f32_e64 v214, v52, v68
	v_add_f32_e64 v215, v53, v69
	v_lshl_add_u32 v202, s89, 14, v115
	v_pk_add_f32 v[212:213], v[214:215], v[212:213]
	v_pk_add_f32 v[214:215], v[54:55], v[70:71]
	ds_read_b128 v[208:211], v174 offset:12288
	ds_read_b128 v[236:239], v174 offset:18432
	v_pk_add_f32 v[212:213], v[214:215], v[212:213]
	s_waitcnt lgkmcnt(7)
	v_mfma_f32_32x32x16_bf16 v[98:113], v[216:219], v[134:137], v[98:113]
	v_add_f32_e64 v214, v56, v72
	v_add_f32_e64 v215, v57, v73
	v_cvt_pk_bf16_f32 v50, v50, v51
	v_cvt_pk_bf16_f32 v51, v52, v53
	v_cvt_pk_bf16_f32 v52, v54, v55
	v_cvt_pk_bf16_f32 v53, v56, v57
	v_cvt_pk_bf16_f32 v54, v58, v59
	v_add_f32_e64 v212, v214, v212
	v_add_f32_e64 v213, v215, v213
	s_waitcnt lgkmcnt(6)
	v_mfma_f32_32x32x16_bf16 v[82:97], v[220:223], v[134:137], v[82:97]
	v_add_f32_e64 v214, v58, v74
	v_add_f32_e64 v215, v59, v75
	v_cvt_pk_bf16_f32 v55, v60, v61
	v_cvt_pk_bf16_f32 v56, v62, v63
	v_cvt_pk_bf16_f32 v57, v64, v65
	v_cvt_pk_bf16_f32 v58, v66, v67
	v_cvt_pk_bf16_f32 v59, v68, v69
	v_add_f32_e64 v212, v214, v212
	v_add_f32_e64 v213, v215, v213
	s_waitcnt lgkmcnt(5)
	v_mfma_f32_32x32x16_bf16 v[98:113], v[124:127], v[130:133], v[98:113]
	v_add_f32_e64 v214, v60, v76
	v_add_f32_e64 v215, v61, v77
	v_add_f32_e64 v126, v62, v78
	v_add_f32_e64 v127, v63, v79
	v_add_f32_e64 v124, v214, v212
	v_add_f32_e64 v125, v215, v213
	v_cvt_pk_bf16_f32 v60, v70, v71
	v_cvt_pk_bf16_f32 v61, v72, v73
	v_cvt_pk_bf16_f32 v62, v74, v75
	v_cvt_pk_bf16_f32 v63, v76, v77
	s_waitcnt lgkmcnt(4)
	v_mfma_f32_32x32x16_bf16 v[82:97], v[224:227], v[130:133], v[82:97]
	v_add_f32_e64 v124, v126, v124
	v_add_f32_e64 v125, v127, v125
	v_add_f32_e64 v126, v64, v80
	v_add_f32_e64 v127, v65, v81
	v_cvt_pk_bf16_f32 v64, v78, v79
	v_cvt_pk_bf16_f32 v65, v80, v81
	ds_read_b64_tr_b16 v[66:67], v202 offset:0
	ds_read_b64_tr_b16 v[68:69], v202 offset:0x400
	ds_read_b64_tr_b16 v[70:71], v202 offset:0x800
	s_waitcnt lgkmcnt(6)
	v_mfma_f32_32x32x16_bf16 v[98:113], v[228:231], v[146:149], v[98:113]
	ds_read_b64_tr_b16 v[72:73], v202 offset:0xc00
	ds_read_b64_tr_b16 v[74:75], v202 offset:0x1000
	ds_read_b64_tr_b16 v[76:77], v202 offset:0x1400
	ds_read_b64_tr_b16 v[78:79], v202 offset:0x1800
	ds_read_b64_tr_b16 v[80:81], v202 offset:0x1c00
	v_add_f32_e64 v124, v126, v124
	v_add_f32_e64 v125, v127, v125
	s_waitcnt lgkmcnt(10)
	v_mfma_f32_32x32x16_bf16 v[82:97], v[232:235], v[146:149], v[82:97]
	v_pk_add_f32 v[124:125], v[124:125], v[124:125] op_sel:[0,1] op_sel_hi:[1,0]
	s_nop 0
	v_mov_b32_e32 v125, v124
	s_nop 1
	v_permlane32_swap_b32_e32 v124, v125
	s_waitcnt lgkmcnt(9)
	v_mfma_f32_32x32x16_bf16 v[98:113], v[208:211], v[142:145], v[98:113]
	ds_read_b64_tr_b16 v[208:209], v202 offset:0x200
	ds_read_b64_tr_b16 v[210:211], v202 offset:0x600
	ds_read_b64_tr_b16 v[212:213], v202 offset:0xa00
	ds_read_b64_tr_b16 v[214:215], v202 offset:0xe00
	ds_read_b64_tr_b16 v[216:217], v202 offset:0x1200
	ds_read_b64_tr_b16 v[218:219], v202 offset:0x1600
	ds_read_b64_tr_b16 v[220:221], v202 offset:0x1a00
	s_waitcnt lgkmcnt(15)
	v_mfma_f32_32x32x16_bf16 v[82:97], v[236:239], v[142:145], v[82:97]
	ds_read_b64_tr_b16 v[222:223], v202 offset:0x1e00
	s_waitcnt lgkmcnt(14)
	v_mfma_f32_32x32x16_bf16 v[18:33], v[50:53], v[66:69], v[18:33]
	s_waitcnt lgkmcnt(12)
	v_mfma_f32_32x32x16_bf16 v[18:33], v[54:57], v[70:73], v[18:33]
	s_waitcnt lgkmcnt(10)
	v_mfma_f32_32x32x16_bf16 v[18:33], v[58:61], v[74:77], v[18:33]
	s_waitcnt lgkmcnt(8)
	v_mfma_f32_32x32x16_bf16 v[18:33], v[62:65], v[78:81], v[18:33]
	s_waitcnt lgkmcnt(6)
	v_mfma_f32_32x32x16_bf16 v[2:17], v[50:53], v[208:211], v[2:17]
	s_nop 4
	v_max_f32_e32 v66, v99, v99
	v_max_f32_e32 v67, v98, v98
	v_max_f32_e32 v66, v67, v66
	v_max3_f32 v66, v66, v100, v101
	v_max3_f32 v66, v66, v102, v103
	v_max3_f32 v50, v66, v104, v105
	v_max3_f32 v50, v50, v106, v107
	s_waitcnt lgkmcnt(4)
	v_mfma_f32_32x32x16_bf16 v[2:17], v[54:57], v[212:215], v[2:17]
	v_max3_f32 v50, v50, v108, v109
	v_max3_f32 v50, v50, v110, v111
	v_max3_f32 v50, v50, v112, v113
	v_max3_f32 v50, v50, v82, v83
	v_max3_f32 v50, v50, v84, v85
	v_max3_f32 v50, v50, v86, v87
	v_max3_f32 v50, v50, v88, v89
	s_waitcnt lgkmcnt(2)
	v_mfma_f32_32x32x16_bf16 v[2:17], v[58:61], v[216:219], v[2:17]
	v_max3_f32 v50, v50, v90, v91
	v_max3_f32 v50, v50, v92, v93
	v_max3_f32 v50, v50, v94, v95
	v_max3_f32 v50, v50, v96, v97
	v_mov_b32_e32 v51, v50
	s_nop 1
	v_permlane32_swap_b32_e32 v50, v51
	s_waitcnt lgkmcnt(0)
	v_mfma_f32_32x32x16_bf16 v[2:17], v[62:65], v[220:223], v[2:17]
	v_max_f32_e32 v51, v51, v51
	v_max_f32_e32 v50, v50, v50
	v_max_f32_e32 v126, v50, v51
	v_cmp_ge_f32_e32 vcc, s79, v126
	s_cmp_lg_u64 vcc, exec
	s_cselect_b64 s[6:7], -1, 0
	s_mov_b64 s[16:17], -1
	s_mov_b64 vcc, s[6:7]
	s_cbranch_vccnz .LBB0_705
	s_andn2_b64 vcc, exec, s[16:17]
	s_cbranch_vccz .LBB0_706

; template <bool FIRST> DEVI bool partialSM(f32x16& p0, f32x16& p1, float& m_reg, float& alpha) {
;     float pmax = p0[0];
; #pragma unroll
;     for (int r = 1; r < 16; ++r) pmax = fmaxf(pmax, p0[r]);
; #pragma unroll
;     for (int r = 0; r < 16; ++r) pmax = fmaxf(pmax, p1[r]);
;     { auto rr = __builtin_amdgcn_permlane32_swap(__float_as_uint(pmax), __float_as_uint(pmax), false, false);
;       pmax = fmaxf(__uint_as_float(rr[0]), __uint_as_float(rr[1])); }
;     if (FIRST) { m_reg = pmax; alpha = 1.f;
; #pragma unroll
;         for (int r = 0; r < 16; ++r) { p0[r] = __builtin_amdgcn_exp2f(p0[r] - pmax); p1[r] = p1[r] - pmax; }
;         return false;
;     } else if (__builtin_expect(__all(pmax <= ATT_THR), 1)) { alpha = 1.f;
; #pragma unroll
;         for (int r = 0; r < 16; ++r) p0[r] = __builtin_amdgcn_exp2f(p0[r]);
;         return false;
;     } else { const float d = fmaxf(pmax, 0.f); alpha = __builtin_amdgcn_exp2f(-d); m_reg += d;
; #pragma unroll
;         for (int r = 0; r < 16; ++r) { p0[r] = __builtin_amdgcn_exp2f(p0[r] - d); p1[r] = p1[r] - d; }
;         return true;
;     }
; }
; DEVI void finishSM(f32x16& p0, f32x16& p1, float alpha, float& l_reg, bf16x8& pa0, bf16x8& pa1, bf16x8& pa2, bf16x8& pa3) {
; #pragma unroll
;     for (int r = 0; r < 16; ++r) p1[r] = __builtin_amdgcn_exp2f(p1[r]);
;     f32x2 s2 = (f32x2){p0[0], p0[1]} + (f32x2){p1[0], p1[1]};
; #pragma unroll
;     for (int r = 2; r < 16; r += 2) s2 += (f32x2){p0[r], p0[r + 1]} + (f32x2){p1[r], p1[r + 1]};
;     float ps = s2[0] + s2[1];
;     { auto rr = __builtin_amdgcn_permlane32_swap(__float_as_uint(ps), __float_as_uint(ps), false, false);
;       ps = __uint_as_float(rr[0]) + __uint_as_float(rr[1]); }
;     l_reg = l_reg * alpha + ps;
;     ...
;     PK4(p0, 0, pa0); PK4(p0, 8, pa1); PK4(p1, 0, pa2); PK4(p1, 8, pa3);
;     ...
; }
; DEVI void qkt(f32x16& p0, f32x16& p1, const char* Kb, const bf16x8 (&qr)[6], int r32, int hi, const f32x16& cinit) {
; #pragma unroll
; DEVI void attn_unit8(const Params& p, char* smem, int unit, int l, int& cvs  , CvRun& crun) {
;     ...
;         if (T + 2 < NTILE) B_DMA(T + 2, s2);
;         qkt(pA0, pA1, K_lds + s1 * 24576, qr, r32, hi, cinit);
;         finishSM(pB0, pB1, alB, l_reg, pa0, pa1, pa2, pa3);
;         pv_both(o[0], o[1], vb + 8192, pa0, pa1, pa2, pa3);
;         { const bool rr_ = partialSM<false>(pA0, pA1, m_reg, alA); B_RESC(alA, rr_); }
.LBB0_702:
	s_mul_i32 s6, s2, 0x6000
	s_add_i32 s6, s96, s6
	v_lshl_add_u64 v[82:83], v[118:119], 0, s[12:13]
	s_mov_b32 m0, s6
	s_barrier
	global_load_lds_dwordx4 v[82:83], off
	v_lshl_add_u64 v[82:83], v[120:121], 0, s[12:13]
	s_add_i32 m0, s6, 0x2000
	v_exp_f32_e32 v66, v66
	global_load_lds_dwordx4 v[82:83], off
	s_add_i32 m0, s6, 0x4000
	s_lshl_b32 s6, s2, 14
	v_lshl_add_u64 v[82:83], v[122:123], 0, s[12:13]
	s_add_i32 s6, s97, s6
	global_load_lds_dwordx4 v[82:83], off
	s_mov_b32 m0, s6
	v_lshl_add_u64 v[82:83], v[116:117], 0, s[40:41]
	global_load_lds_dwordx4 v[116:117], off
	s_add_i32 m0, s6, 0x2000
	s_mul_i32 s6, s61, 0x6000
	global_load_lds_dwordx4 v[82:83], off
	s_add_i32 s6, s6, 0
	v_add_u32_e32 v86, s6, v129
	ds_read_b128 v[82:85], v86
	ds_read_b128 v[210:213], v86 offset:6144
	s_waitcnt lgkmcnt(1)
	v_mfma_f32_32x32x16_bf16 v[98:113], v[82:85], v[150:153], v[34:49]
	v_add_u32_e32 v126, s6, v184
	v_exp_f32_e32 v67, v67
	v_exp_f32_e32 v68, v68
	v_exp_f32_e32 v69, v69
	v_exp_f32_e32 v70, v70
	v_exp_f32_e32 v71, v71
	v_exp_f32_e32 v72, v72
	s_waitcnt lgkmcnt(0)
	v_mfma_f32_32x32x16_bf16 v[82:97], v[210:213], v[150:153], v[34:49]
	ds_read_b128 v[210:213], v126
	ds_read_b128 v[214:217], v126 offset:6144
	v_add_u32_e32 v126, s6, v185
	v_exp_f32_e32 v73, v73
	v_exp_f32_e32 v74, v74
	v_exp_f32_e32 v75, v75
	v_exp_f32_e32 v76, v76
	v_exp_f32_e32 v77, v77
	s_waitcnt lgkmcnt(1)
	v_mfma_f32_32x32x16_bf16 v[98:113], v[210:213], v[138:141], v[98:113]
	v_exp_f32_e32 v78, v78
	v_exp_f32_e32 v79, v79
	v_exp_f32_e32 v80, v80
	v_exp_f32_e32 v81, v81
	v_add_u32_e32 v174, 0x2000, v202
	s_waitcnt lgkmcnt(0)
	v_mfma_f32_32x32x16_bf16 v[82:97], v[214:217], v[138:141], v[82:97]
	ds_read_b128 v[210:213], v126
	ds_read_b128 v[214:217], v126 offset:6144
	v_add_u32_e32 v126, s6, v204
	s_waitcnt lgkmcnt(1)
	v_mfma_f32_32x32x16_bf16 v[98:113], v[210:213], v[134:137], v[98:113]
	ds_read_b128 v[210:213], v126
	ds_read_b128 v[218:221], v126 offset:6144
	v_add_u32_e32 v126, s6, v205
	s_waitcnt lgkmcnt(2)
	v_mfma_f32_32x32x16_bf16 v[82:97], v[214:217], v[134:137], v[82:97]
	ds_read_b128 v[214:217], v126
	ds_read_b128 v[222:225], v126 offset:6144
	v_add_u32_e32 v126, s6, v206
	ds_read_b128 v[226:229], v126
	ds_read_b128 v[230:233], v126 offset:6144
	v_pk_add_f32 v[126:127], v[50:51], v[66:67]
	v_cvt_pk_bf16_f32 v50, v50, v51
	v_cvt_pk_bf16_f32 v51, v52, v53
	s_waitcnt lgkmcnt(5)
	v_mfma_f32_32x32x16_bf16 v[98:113], v[210:213], v[130:133], v[98:113]
	v_add_f32_e64 v210, v52, v68
	v_add_f32_e64 v211, v53, v69
	v_cvt_pk_bf16_f32 v52, v54, v55
	v_cvt_pk_bf16_f32 v53, v56, v57
	v_add_f32_e64 v126, v210, v126
	v_add_f32_e64 v127, v211, v127
	v_add_f32_e64 v210, v54, v70
	v_add_f32_e64 v211, v55, v71
	v_cvt_pk_bf16_f32 v54, v58, v59
	s_waitcnt lgkmcnt(4)
	v_mfma_f32_32x32x16_bf16 v[82:97], v[218:221], v[130:133], v[82:97]
	v_add_f32_e64 v126, v210, v126
	v_add_f32_e64 v127, v211, v127
	v_add_f32_e64 v210, v56, v72
	v_add_f32_e64 v211, v57, v73
	v_cvt_pk_bf16_f32 v55, v60, v61
	v_cvt_pk_bf16_f32 v56, v62, v63
	v_cvt_pk_bf16_f32 v57, v64, v65
	v_add_f32_e64 v126, v210, v126
	v_add_f32_e64 v127, v211, v127
	v_pk_add_f32 v[210:211], v[58:59], v[74:75]
	v_cvt_pk_bf16_f32 v58, v66, v67
	v_cvt_pk_bf16_f32 v59, v68, v69
	s_waitcnt lgkmcnt(3)
	v_mfma_f32_32x32x16_bf16 v[98:113], v[214:217], v[146:149], v[98:113]
	v_add_f32_e64 v126, v210, v126
	v_add_f32_e64 v127, v211, v127
	v_add_f32_e64 v210, v60, v76
	v_add_f32_e64 v211, v61, v77
	v_cvt_pk_bf16_f32 v60, v70, v71
	v_cvt_pk_bf16_f32 v61, v72, v73
	v_add_f32_e64 v126, v210, v126
	v_add_f32_e64 v127, v211, v127
	v_pk_add_f32 v[210:211], v[62:63], v[78:79]
	v_cvt_pk_bf16_f32 v62, v74, v75
	v_cvt_pk_bf16_f32 v63, v76, v77
	s_waitcnt lgkmcnt(2)
	v_mfma_f32_32x32x16_bf16 v[82:97], v[222:225], v[146:149], v[82:97]
	v_add_f32_e64 v126, v210, v126
	v_add_f32_e64 v127, v211, v127
	v_add_f32_e64 v210, v64, v80
	v_add_f32_e64 v211, v65, v81
	v_cvt_pk_bf16_f32 v64, v78, v79
	v_cvt_pk_bf16_f32 v65, v80, v81
	ds_read_b64_tr_b16 v[66:67], v174 offset:0
	ds_read_b64_tr_b16 v[68:69], v174 offset:0x400
	ds_read_b64_tr_b16 v[70:71], v174 offset:0x800
	ds_read_b64_tr_b16 v[72:73], v174 offset:0xc00
	ds_read_b64_tr_b16 v[74:75], v174 offset:0x1000
	ds_read_b64_tr_b16 v[76:77], v174 offset:0x1400
	ds_read_b64_tr_b16 v[78:79], v174 offset:0x1800
	ds_read_b64_tr_b16 v[80:81], v174 offset:0x1c00
	v_add_f32_e64 v126, v210, v126
	v_add_f32_e64 v127, v211, v127
	ds_read_b64_tr_b16 v[210:211], v174 offset:0x200
	ds_read_b64_tr_b16 v[212:213], v174 offset:0x600
	ds_read_b64_tr_b16 v[214:215], v174 offset:0xa00
	s_waitcnt lgkmcnt(12)
	v_mfma_f32_32x32x16_bf16 v[98:113], v[226:229], v[142:145], v[98:113]
	ds_read_b64_tr_b16 v[216:217], v174 offset:0xe00
	ds_read_b64_tr_b16 v[218:219], v174 offset:0x1200
	ds_read_b64_tr_b16 v[220:221], v174 offset:0x1600
	ds_read_b64_tr_b16 v[222:223], v174 offset:0x1a00
	ds_read_b64_tr_b16 v[224:225], v174 offset:0x1e00
	v_pk_add_f32 v[126:127], v[126:127], v[126:127] op_sel:[0,1] op_sel_hi:[1,0]
	s_waitcnt lgkmcnt(15)
	v_mfma_f32_32x32x16_bf16 v[82:97], v[230:233], v[142:145], v[82:97]
	v_mov_b32_e32 v127, v126
	s_nop 1
	v_permlane32_swap_b32_e32 v126, v127
	s_waitcnt lgkmcnt(14)
	v_mfma_f32_32x32x16_bf16 v[18:33], v[50:53], v[66:69], v[18:33]
	s_waitcnt lgkmcnt(12)
	v_mfma_f32_32x32x16_bf16 v[18:33], v[54:57], v[70:73], v[18:33]
	s_waitcnt lgkmcnt(10)
	v_mfma_f32_32x32x16_bf16 v[18:33], v[58:61], v[74:77], v[18:33]
	s_waitcnt lgkmcnt(8)
	v_mfma_f32_32x32x16_bf16 v[18:33], v[62:65], v[78:81], v[18:33]
	s_waitcnt lgkmcnt(6)
	v_mfma_f32_32x32x16_bf16 v[2:17], v[50:53], v[210:213], v[2:17]
	s_nop 0
	v_max_f32_e32 v66, v99, v99
	v_max_f32_e32 v67, v98, v98
	v_max_f32_e32 v66, v67, v66
	v_max3_f32 v66, v66, v100, v101
	v_max3_f32 v66, v66, v102, v103
	v_max3_f32 v50, v66, v104, v105
	v_max3_f32 v50, v50, v106, v107
	s_waitcnt lgkmcnt(4)
	v_mfma_f32_32x32x16_bf16 v[2:17], v[54:57], v[214:217], v[2:17]
	v_max3_f32 v50, v50, v108, v109
	v_max3_f32 v50, v50, v110, v111
	v_max3_f32 v50, v50, v112, v113
	v_max3_f32 v50, v50, v82, v83
	v_max3_f32 v50, v50, v84, v85
	v_max3_f32 v50, v50, v86, v87
	v_max3_f32 v50, v50, v88, v89
	s_waitcnt lgkmcnt(2)
	v_mfma_f32_32x32x16_bf16 v[2:17], v[58:61], v[218:221], v[2:17]
	v_max3_f32 v50, v50, v90, v91
	v_max3_f32 v50, v50, v92, v93
	v_max3_f32 v50, v50, v94, v95
	v_max3_f32 v50, v50, v96, v97
	v_mov_b32_e32 v51, v50
	s_nop 1
	v_permlane32_swap_b32_e32 v50, v51
	s_waitcnt lgkmcnt(0)
	v_mfma_f32_32x32x16_bf16 v[2:17], v[62:65], v[222:225], v[2:17]
	v_max_f32_e32 v51, v51, v51
	v_max_f32_e32 v50, v50, v50
	v_max_f32_e32 v174, v50, v51
	v_cmp_ge_f32_e32 vcc, s79, v174
	s_cmp_lg_u64 vcc, exec
	s_cselect_b64 s[6:7], -1, 0
	s_mov_b64 s[14:15], -1
	s_mov_b64 vcc, s[6:7]
	s_cbranch_vccnz .LBB0_711
	s_andn2_b64 vcc, exec, s[14:15]
	s_cbranch_vccz .LBB0_712

; DEVI unsigned xb_add(unsigned* p, unsigned v) { return __hip_atomic_fetch_add(p, v, __ATOMIC_RELAXED, __HIP_MEMORY_SCOPE_AGENT); }
; DEVI void xcd_barrier(const XcdBarrier& b) {
;     asm volatile("s_waitcnt vmcnt(0)" ::: "memory");
;     __syncthreads();
;     if (threadIdx.x == 0) {
;         unsigned* bar = b.bar;
;         __builtin_amdgcn_s_waitcnt(0);
;         unsigned nloc = b.st[0], nx = b.st[1];
;         if (nloc == 0u) { xcd_barrier_complete(bar, b.x, nloc, nx); b.st[0] = nloc; b.st[1] = nx; }
;         const unsigned old = xb_add(&bar[XB_XSUB(b.x)], 1u);
.LBB0_810:
	s_setprio 0
	s_mov_b64 s[6:7], s[0:1]
	s_getreg_b32 s2, hwreg(HW_REG_XCC_ID, 0, 4)
	s_waitcnt vmcnt(0)
	s_barrier
	s_mov_b64 s[4:5], exec
	v_readlane_b32 s8, v248, 0
	v_readlane_b32 s9, v248, 1
	s_and_b64 s[8:9], s[4:5], s[8:9]
	s_mov_b64 exec, s[8:9]
	s_cbranch_execz .LBB0_862
	s_add_i32 s8, 0, 0x258f0
	v_mov_b32_e32 v1, s8
	s_load_dwordx2 s[6:7], s[6:7], 0xf8
	s_waitcnt vmcnt(0) expcnt(0) lgkmcnt(0)
	ds_read_b32 v3, v1
	s_add_i32 s8, 0, 0x258f4
	v_mov_b32_e32 v1, s8
	ds_read_b32 v1, v1
	s_and_b32 s2, s2, 15
	s_waitcnt lgkmcnt(1)
	v_cmp_ne_u32_e32 vcc, 0, v3
	s_cbranch_vccnz .LBB0_826
	v_readlane_b32 s8, v248, 2
	v_readlane_b32 s9, v248, 3
	s_load_dwordx2 s[12:13], s[8:9], 0x4
	s_add_u32 s8, s6, 0x1000
	s_addc_u32 s9, s7, 0
	s_add_u32 s10, s6, 0x1100
	s_addc_u32 s11, s7, 0
	s_waitcnt lgkmcnt(0)
	s_mul_i32 s22, s12, s33
	s_add_u32 s12, s6, 0x1200
	s_mul_i32 s22, s22, s13
	s_addc_u32 s13, s7, 0
	s_add_u32 s14, s6, 0x1300
	s_addc_u32 s15, s7, 0
	s_mov_b32 s23, 1
	v_mov_b32_e32 v17, 0
	s_branch .LBB0_814

; DEVI void phase_combine(const Params& p, char* smem, int l) {
;     ...
;     for (int t = gw; t < T_; t += nw) {
;         const int b = t >> 12;
;         const size_t slot = slot_nx;
;         { const int tn = t + nw; slot_nx = (size_t)T_ * 8 + tn;
;           if (lane < 8 && tn < T_) slot_nx = (size_t)mt.rstart[tke[tn * 8 + lane]] + tkp[tn * 8 + lane]; }
;         u32x4 w[9];
; #pragma unroll
;         for (int k = 0; k < 9; ++k) { const size_t sl = (size_t)(unsigned)__builtin_amdgcn_readlane((int)(unsigned)slot, k);
;             w[k] = *(const u32x4*)(ysl + sl * 1024 + lane * 16); }
;         const u32x4 xr0 = *(const u32x4*)(xab + (size_t)t * 1024 + lane * 16), xr1 = *(const u32x4*)(xab + (size_t)t * 1024 + lane * 16 + 8);
.LBB0_1732:
	v_add_u32_e32 v135, s86, v137
	v_cmp_gt_i32_e64 s[6:7], s38, v135
	v_add_u32_e32 v133, 0x40000, v135
	v_cmp_lt_i32_e32 vcc, s35, v135
	s_and_b64 s[42:43], s[4:5], s[6:7]
	s_and_b64 s[6:7], exec, vcc
	s_or_b64 s[20:21], s[6:7], s[20:21]
	v_readlane_b32 s22, v82, 0
	s_lshl_b64 s[6:7], s[22:23], 10
	v_readlane_b32 s22, v82, 1
	v_lshl_add_u64 v[84:85], v[128:129], 0, s[6:7]
	s_lshl_b64 s[6:7], s[22:23], 10
	v_readlane_b32 s22, v82, 2
	v_lshl_add_u64 v[86:87], v[128:129], 0, s[6:7]
	s_lshl_b64 s[6:7], s[22:23], 10
	v_readlane_b32 s22, v82, 3
	flat_load_dwordx4 v[122:125], v[84:85]
	flat_load_dwordx4 v[114:117], v[86:87]
	v_lshl_add_u64 v[84:85], v[128:129], 0, s[6:7]
	s_lshl_b64 s[6:7], s[22:23], 10
	v_readlane_b32 s22, v82, 4
	v_lshl_add_u64 v[86:87], v[128:129], 0, s[6:7]
	s_lshl_b64 s[6:7], s[22:23], 10
	v_readlane_b32 s22, v82, 5
	flat_load_dwordx4 v[118:121], v[84:85]
	flat_load_dwordx4 v[106:109], v[86:87]
	v_lshl_add_u64 v[84:85], v[128:129], 0, s[6:7]
	s_lshl_b64 s[6:7], s[22:23], 10
	v_readlane_b32 s22, v82, 6
	v_lshl_add_u64 v[86:87], v[128:129], 0, s[6:7]
	s_lshl_b64 s[6:7], s[22:23], 10
	v_readlane_b32 s22, v82, 7
	flat_load_dwordx4 v[110:113], v[84:85]
	flat_load_dwordx4 v[98:101], v[86:87]
	v_lshl_add_u64 v[84:85], v[128:129], 0, s[6:7]
	s_lshl_b64 s[6:7], s[22:23], 10
	v_readlane_b32 s22, v82, 8
	v_lshl_add_u64 v[86:87], v[128:129], 0, s[6:7]
	s_lshl_b64 s[6:7], s[22:23], 10
	v_lshl_add_u64 v[82:83], v[128:129], 0, s[6:7]
	flat_load_dwordx4 v[102:105], v[84:85]
	flat_load_dwordx4 v[94:97], v[86:87]
	flat_load_dwordx4 v[90:93], v[82:83]
	v_lshl_add_u64 v[82:83], s[10:11], 0, v[130:131]
	flat_load_dwordx4 v[86:89], v[82:83]
	s_nop 0
	flat_load_dwordx4 v[82:85], v[82:83] offset:16
	s_and_saveexec_b64 s[6:7], s[42:43]
	s_cbranch_execz .Lmy_cmb_skip_a
	v_ashrrev_i32_e32 v133, 31, v132
	v_lshlrev_b64 v[250:251], 2, v[132:133]
	v_lshl_add_u64 v[252:253], s[12:13], 0, v[250:251]
	flat_load_dword v254, v[252:253]
	v_lshl_add_u64 v[250:251], s[14:15], 0, v[250:251]
	flat_load_dword v255, v[250:251]
	s_waitcnt vmcnt(0) lgkmcnt(0)
	v_lshl_add_u32 v254, v254, 2, s2
	ds_read_b32 v254, v254 offset:61440
	s_waitcnt lgkmcnt(0)
	v_add_u32_e32 v133, v255, v254
.Lmy_cmb_skip_a:
	s_or_b64 exec, exec, s[6:7]
	v_ashrrev_i32_e32 v137, 12, v137
	v_cmp_ne_u32_e32 vcc, v137, v136
	s_and_saveexec_b64 s[6:7], vcc
	s_cbranch_execz .LBB0_1731
	s_load_dwordx2 s[42:43], s[16:17], 0x108
	v_mul_hi_i32_i24_e32 v35, 0x6000, v137
	v_mul_i32_i24_e32 v34, 0x6000, v137
	v_mov_b32_e32 v136, v137
	s_waitcnt lgkmcnt(0)
	v_lshl_add_u64 v[34:35], s[42:43], 0, v[34:35]
	v_lshl_add_u64 v[66:67], v[34:35], 0, v[126:127]
	v_add_co_u32_e32 v34, vcc, 0x5000, v66
	v_lshl_add_u64 v[38:39], v[66:67], 0, s[24:25]
	s_nop 0
	v_addc_co_u32_e32 v35, vcc, 0, v67, vcc
	v_add_co_u32_e32 v50, vcc, s39, v66
	v_lshl_add_u64 v[54:55], v[66:67], 0, s[26:27]
	s_nop 0
	v_addc_co_u32_e32 v51, vcc, 0, v67, vcc
	v_lshl_add_u64 v[74:75], v[66:67], 0, s[28:29]
	v_add_co_u32_e32 v66, vcc, 0x31000, v66
	global_load_dwordx4 v[34:37], v[34:35], off
	s_nop 0
	global_load_dwordx4 v[46:49], v[38:39], off offset:48
	global_load_dwordx4 v[42:45], v[38:39], off offset:32
	s_nop 0
	global_load_dwordx4 v[38:41], v[38:39], off offset:16
	v_addc_co_u32_e32 v67, vcc, 0, v67, vcc
	global_load_dwordx4 v[50:53], v[50:51], off
	s_nop 0
	global_load_dwordx4 v[62:65], v[54:55], off offset:48
	global_load_dwordx4 v[58:61], v[54:55], off offset:32
	s_nop 0
	global_load_dwordx4 v[54:57], v[54:55], off offset:16
	s_nop 0
	global_load_dwordx4 v[70:73], v[66:67], off
	global_load_dwordx4 v[78:81], v[74:75], off offset:48
	s_nop 0
	global_load_dwordx4 v[66:69], v[74:75], off offset:32
	s_nop 0
	global_load_dwordx4 v[74:77], v[74:75], off offset:16
	s_branch .LBB0_1731

; DEVI int tidx() { int t = threadIdx.x; asm volatile("" : "+v"(t)); __builtin_assume(t >= 0 && t < 512); return t; }
; DEVI int bidx() { int b = blockIdx.x; asm volatile("" : "+s"(b)); __builtin_assume(b >= 0 && b < 65536); return b; }
; DEVI void attn_unit8(const Params& p, char* smem, int unit, int l, int& cvs  , CvRun& crun) {
;     const int tid = tidx(), wid = __builtin_amdgcn_readfirstlane(tid >> 6), lane = tid & 63, r32 = lane & 31, hi = lane >> 5;
;     const int x8 = unit & 7, v8 = unit >> 3, bh = x8 + 8 * (v8 >> 4), qt = v8 & 15, b = bh >> 3, hh = bh & 7;
;     char* K_lds = smem; char* V_lds = smem + 73728;
;     float* wsx = (float*)(smem + 122880) + wid * 64; float* li_l = wsx; float* al_l = wsx + 32;
;     const bf16_t* Kg = p.kfull + (size_t)bh * S_ * 96; const bf16_t* Vg = p.vfull + (size_t)bh * S_ * 64;
;     const size_t qtok = (size_t)b * S_ + qt * 256 + wid * 32 + r32;
; DEVI void phase_attn(const Params& p, char* smem, int l) {
;     mlstm_scan(p);
;     const int lane = tidx() & 63, wid = __builtin_amdgcn_readfirstlane(tidx() >> 6);
;     int cvs = bidx() * 8 + wid;
;     CvRun crun; crun.left = 0; crun.sstep = 0; crun.dstep = 0;
;     for (int u = bidx(); u < 64 * 16; u += gridDim.x) attn_unit8(p, smem, u, l, cvs, crun);
.LBB0_2226:
	s_or_b64 exec, exec, s[16:17]
	v_mov_b32_e32 v177, v0
	v_mov_b32_e32 v2, v0
	s_mov_b32 s62, s84
	v_readfirstlane_b32 s2, v2
	s_lshr_b32 s4, s2, 6
	s_mov_b32 s2, s84
	s_lshl_b32 s2, s2, 3
	s_add_i32 s54, s2, s4
	s_cmpk_gt_u32 s62, 0x3ff
	v_writelane_b32 v248, s4, 6
	s_cbranch_scc1 .LBB0_2342
	v_readlane_b32 s98, v248, 6
	s_nop 3
	s_cmp_lt_u32 s98, 4
	s_cbranch_scc1 .Lmy_prio_b
	s_setprio 1
.Lmy_prio_b:
	s_and_b32 s2, s33, 63
	s_cmp_eq_u32 s2, 0
	s_cselect_b64 s[30:31], -1, 0
	s_ashr_i32 s4, s33, 5
	s_abs_i32 s63, s4
	v_cvt_f32_u32_e32 v2, s63
	s_ashr_i32 s5, s4, 31
	s_lshl_b64 s[34:35], s[4:5], 18
	s_ashr_i32 s4, s33, 6
	v_rcp_iflag_f32_e32 v2, v2
	s_abs_i32 s64, s4
	v_cvt_f32_u32_e32 v3, s64
	s_ashr_i32 s5, s4, 31
	v_mul_f32_e32 v2, 0x4f7ffffe, v2
	v_cvt_u32_f32_e32 v2, v2
	v_rcp_iflag_f32_e32 v3, v3
	s_lshl_b64 s[36:37], s[4:5], 18
	s_lshl_b64 s[38:39], s[4:5], 19
	v_readfirstlane_b32 s4, v2
	v_mul_f32_e32 v2, 0x4f7ffffe, v3
	v_cvt_u32_f32_e32 v2, v2
	s_sub_i32 s2, 0, s63
	s_mul_i32 s2, s2, s4
	s_mul_hi_u32 s2, s4, s2
	s_add_i32 s65, s4, s2
	s_sub_i32 s2, 0, s64
	v_readfirstlane_b32 s4, v2
	s_mul_i32 s2, s2, s4
	s_mul_hi_u32 s2, s4, s2
	s_mov_b32 s9, 0
	s_add_i32 s66, s4, s2
	s_lshl_b32 s67, s33, 13
	s_lshl_b32 s68, s33, 8
	s_lshl_b32 s69, s33, 7
	s_lshl_b32 s72, s33, 6
	s_lshl_b32 s73, s33, 4
	s_mov_b64 s[26:27], 0
	v_mov_b32_e32 v175, 0
	s_movk_i32 s74, 0x600
	v_mov_b32_e32 v181, 0x600
	s_mov_b32 s75, 0xaaab
	s_add_i32 s76, 0, 0x12000
	s_mov_b64 s[40:41], 0x2000
	s_mov_b64 s[42:43], 0x6000
	s_mov_b64 s[44:45], 0x4000
	s_movk_i32 s77, 0x80
	s_movk_i32 s78, 0x44
	s_mov_b64 s[46:47], 0x8000
	s_movk_i32 s79, 0xd8
	s_mov_b32 s80, 0x41000000
	s_add_i32 s81, 0, 0x14000
	s_add_i32 s82, 0, 0x16000
	s_add_i32 s83, 0, 0x18000
	v_mov_b32_e32 v186, 0x41800000
	s_mov_b32 s87, s62
	s_mov_b64 s[28:29], 0
	s_mov_b32 s56, 0
	s_branch .LBB0_2229

; template <bool FIRST> DEVI bool partialSM(f32x16& p0, f32x16& p1, float& m_reg, float& alpha) {
;     float pmax = p0[0];
; #pragma unroll
;     for (int r = 1; r < 16; ++r) pmax = fmaxf(pmax, p0[r]);
; #pragma unroll
;     for (int r = 0; r < 16; ++r) pmax = fmaxf(pmax, p1[r]);
;     { auto rr = __builtin_amdgcn_permlane32_swap(__float_as_uint(pmax), __float_as_uint(pmax), false, false);
;       pmax = fmaxf(__uint_as_float(rr[0]), __uint_as_float(rr[1])); }
;     if (FIRST) { m_reg = pmax; alpha = 1.f;
; #pragma unroll
;         for (int r = 0; r < 16; ++r) { p0[r] = __builtin_amdgcn_exp2f(p0[r] - pmax); p1[r] = p1[r] - pmax; }
;         return false;
;     } else if (__builtin_expect(__all(pmax <= ATT_THR), 1)) { alpha = 1.f;
; #pragma unroll
;         for (int r = 0; r < 16; ++r) p0[r] = __builtin_amdgcn_exp2f(p0[r]);
;         return false;
;     } else { const float d = fmaxf(pmax, 0.f); alpha = __builtin_amdgcn_exp2f(-d); m_reg += d;
; #pragma unroll
;         for (int r = 0; r < 16; ++r) { p0[r] = __builtin_amdgcn_exp2f(p0[r] - d); p1[r] = p1[r] - d; }
;         return true;
;     }
; }
; DEVI void finishSM(f32x16& p0, f32x16& p1, float alpha, float& l_reg, bf16x8& pa0, bf16x8& pa1, bf16x8& pa2, bf16x8& pa3) {
; #pragma unroll
;     for (int r = 0; r < 16; ++r) p1[r] = __builtin_amdgcn_exp2f(p1[r]);
;     f32x2 s2 = (f32x2){p0[0], p0[1]} + (f32x2){p1[0], p1[1]};
; #pragma unroll
;     for (int r = 2; r < 16; r += 2) s2 += (f32x2){p0[r], p0[r + 1]} + (f32x2){p1[r], p1[r + 1]};
;     float ps = s2[0] + s2[1];
;     { auto rr = __builtin_amdgcn_permlane32_swap(__float_as_uint(ps), __float_as_uint(ps), false, false);
;       ps = __uint_as_float(rr[0]) + __uint_as_float(rr[1]); }
;     l_reg = l_reg * alpha + ps;
;     ...
;     PK4(p0, 0, pa0); PK4(p0, 8, pa1); PK4(p1, 0, pa2); PK4(p1, 8, pa3);
;     ...
; }
; DEVI void qkt(f32x16& p0, f32x16& p1, const char* Kb, const bf16x8 (&qr)[6], int r32, int hi, const f32x16& cinit) {
; #pragma unroll
;     for (int d0 = 0; d0 < 6; ++d0) { const int cb = (d0 * 16 + hi * 8) * 2;
;         const bf16x8 k0 = *(const bf16x8*)(Kb + KSWZ(r32, cb)), k1 = *(const bf16x8*)(Kb + KSWZ(32 + r32, cb));
;         p0 = __builtin_amdgcn_mfma_f32_32x32x16_bf16(k0, qr[d0], d0 == 0 ? cinit : p0, 0, 0, 0);
;         p1 = __builtin_amdgcn_mfma_f32_32x32x16_bf16(k1, qr[d0], d0 == 0 ? cinit : p1, 0, 0, 0); }
; }
.LBB0_2260:
	s_mul_i32 s6, s71, 0x6000
	s_add_i32 s6, s6, 0
	v_add_u32_e32 v86, s6, v129
	ds_read_b128 v[82:85], v86 offset:12288
	ds_read_b128 v[124:127], v86 offset:18432
	v_add_u32_e32 v174, s6, v205
	v_exp_f32_e32 v66, v66
	v_exp_f32_e32 v67, v67
	s_waitcnt lgkmcnt(1)
	v_mfma_f32_32x32x16_bf16 v[98:113], v[82:85], v[150:153], v[34:49]
	v_add_u32_e32 v82, s6, v184
	v_add_u32_e32 v83, s6, v185
	ds_read_b128 v[210:213], v82 offset:12288
	ds_read_b128 v[214:217], v82 offset:18432
	ds_read_b128 v[218:221], v83 offset:12288
	ds_read_b128 v[222:225], v83 offset:18432
	v_exp_f32_e32 v68, v68
	v_exp_f32_e32 v69, v69
	v_exp_f32_e32 v70, v70
	v_exp_f32_e32 v71, v71
	s_waitcnt lgkmcnt(4)
	v_mfma_f32_32x32x16_bf16 v[82:97], v[124:127], v[150:153], v[34:49]
	ds_read_b128 v[124:127], v174 offset:12288
	ds_read_b128 v[226:229], v174 offset:18432
	v_exp_f32_e32 v72, v72
	v_exp_f32_e32 v73, v73
	v_exp_f32_e32 v74, v74
	v_exp_f32_e32 v75, v75
	v_exp_f32_e32 v76, v76
	v_exp_f32_e32 v77, v77
	s_waitcnt lgkmcnt(5)
	v_mfma_f32_32x32x16_bf16 v[98:113], v[210:213], v[138:141], v[98:113]
	v_add_u32_e32 v174, s6, v206
	v_exp_f32_e32 v78, v78
	v_exp_f32_e32 v79, v79
	ds_read_b128 v[230:233], v174 offset:12288
	ds_read_b128 v[234:237], v174 offset:18432
	v_exp_f32_e32 v80, v80
	v_exp_f32_e32 v81, v81
	v_add_u32_e32 v174, s6, v207
	s_waitcnt lgkmcnt(6)
	v_mfma_f32_32x32x16_bf16 v[82:97], v[214:217], v[138:141], v[82:97]
	v_add_f32_e64 v214, v50, v66
	v_add_f32_e64 v215, v51, v67
	v_add_f32_e64 v216, v52, v68
	v_add_f32_e64 v217, v53, v69
	v_lshl_add_u32 v203, s71, 14, v115
	v_pk_add_f32 v[214:215], v[216:217], v[214:215]
	v_pk_add_f32 v[216:217], v[54:55], v[70:71]
	ds_read_b128 v[210:213], v174 offset:12288
	ds_read_b128 v[238:241], v174 offset:18432
	v_pk_add_f32 v[214:215], v[216:217], v[214:215]
	s_waitcnt lgkmcnt(7)
	v_mfma_f32_32x32x16_bf16 v[98:113], v[218:221], v[134:137], v[98:113]
	v_add_f32_e64 v216, v56, v72
	v_add_f32_e64 v217, v57, v73
	v_cvt_pk_bf16_f32 v50, v50, v51
	v_cvt_pk_bf16_f32 v51, v52, v53
	v_cvt_pk_bf16_f32 v52, v54, v55
	v_cvt_pk_bf16_f32 v53, v56, v57
	v_cvt_pk_bf16_f32 v54, v58, v59
	v_add_f32_e64 v214, v216, v214
	v_add_f32_e64 v215, v217, v215
	s_waitcnt lgkmcnt(6)
	v_mfma_f32_32x32x16_bf16 v[82:97], v[222:225], v[134:137], v[82:97]
	v_add_f32_e64 v216, v58, v74
	v_add_f32_e64 v217, v59, v75
	v_cvt_pk_bf16_f32 v55, v60, v61
	v_cvt_pk_bf16_f32 v56, v62, v63
	v_cvt_pk_bf16_f32 v57, v64, v65
	v_cvt_pk_bf16_f32 v58, v66, v67
	v_cvt_pk_bf16_f32 v59, v68, v69
	v_add_f32_e64 v214, v216, v214
	v_add_f32_e64 v215, v217, v215
	s_waitcnt lgkmcnt(5)
	v_mfma_f32_32x32x16_bf16 v[98:113], v[124:127], v[130:133], v[98:113]
	v_add_f32_e64 v216, v60, v76
	v_add_f32_e64 v217, v61, v77
	v_add_f32_e64 v126, v62, v78
	v_add_f32_e64 v127, v63, v79
	v_add_f32_e64 v124, v216, v214
	v_add_f32_e64 v125, v217, v215
	v_cvt_pk_bf16_f32 v60, v70, v71
	v_cvt_pk_bf16_f32 v61, v72, v73
	v_cvt_pk_bf16_f32 v62, v74, v75
	v_cvt_pk_bf16_f32 v63, v76, v77
	s_waitcnt lgkmcnt(4)
	v_mfma_f32_32x32x16_bf16 v[82:97], v[226:229], v[130:133], v[82:97]
	v_add_f32_e64 v124, v126, v124
	v_add_f32_e64 v125, v127, v125
	v_add_f32_e64 v126, v64, v80
	v_add_f32_e64 v127, v65, v81
	v_cvt_pk_bf16_f32 v64, v78, v79
	v_cvt_pk_bf16_f32 v65, v80, v81
	ds_read_b64_tr_b16 v[66:67], v203 offset:0
	ds_read_b64_tr_b16 v[68:69], v203 offset:0x400
	ds_read_b64_tr_b16 v[70:71], v203 offset:0x800
	s_waitcnt lgkmcnt(6)
	v_mfma_f32_32x32x16_bf16 v[98:113], v[230:233], v[146:149], v[98:113]
	ds_read_b64_tr_b16 v[72:73], v203 offset:0xc00
	ds_read_b64_tr_b16 v[74:75], v203 offset:0x1000
	ds_read_b64_tr_b16 v[76:77], v203 offset:0x1400
	ds_read_b64_tr_b16 v[78:79], v203 offset:0x1800
	ds_read_b64_tr_b16 v[80:81], v203 offset:0x1c00
	v_add_f32_e64 v124, v126, v124
	v_add_f32_e64 v125, v127, v125
	s_waitcnt lgkmcnt(10)
	v_mfma_f32_32x32x16_bf16 v[82:97], v[234:237], v[146:149], v[82:97]
	v_pk_add_f32 v[124:125], v[124:125], v[124:125] op_sel:[0,1] op_sel_hi:[1,0]
	s_nop 0
	v_mov_b32_e32 v125, v124
	s_nop 1
	v_permlane32_swap_b32_e32 v124, v125
	s_waitcnt lgkmcnt(9)
	v_mfma_f32_32x32x16_bf16 v[98:113], v[210:213], v[142:145], v[98:113]
	ds_read_b64_tr_b16 v[210:211], v203 offset:0x200
	ds_read_b64_tr_b16 v[212:213], v203 offset:0x600
	ds_read_b64_tr_b16 v[214:215], v203 offset:0xa00
	ds_read_b64_tr_b16 v[216:217], v203 offset:0xe00
	ds_read_b64_tr_b16 v[218:219], v203 offset:0x1200
	ds_read_b64_tr_b16 v[220:221], v203 offset:0x1600
	ds_read_b64_tr_b16 v[222:223], v203 offset:0x1a00
	s_waitcnt lgkmcnt(15)
	v_mfma_f32_32x32x16_bf16 v[82:97], v[238:241], v[142:145], v[82:97]
	ds_read_b64_tr_b16 v[224:225], v203 offset:0x1e00
	s_waitcnt lgkmcnt(14)
	v_mfma_f32_32x32x16_bf16 v[18:33], v[50:53], v[66:69], v[18:33]
	s_waitcnt lgkmcnt(12)
	v_mfma_f32_32x32x16_bf16 v[18:33], v[54:57], v[70:73], v[18:33]
	s_waitcnt lgkmcnt(10)
	v_mfma_f32_32x32x16_bf16 v[18:33], v[58:61], v[74:77], v[18:33]
	s_waitcnt lgkmcnt(8)
	v_mfma_f32_32x32x16_bf16 v[18:33], v[62:65], v[78:81], v[18:33]
	s_waitcnt lgkmcnt(6)
	v_mfma_f32_32x32x16_bf16 v[2:17], v[50:53], v[210:213], v[2:17]
	s_nop 4
	v_max_f32_e32 v66, v99, v99
	v_max_f32_e32 v67, v98, v98
	v_max_f32_e32 v66, v67, v66
	v_max3_f32 v66, v66, v100, v101
	v_max3_f32 v66, v66, v102, v103
	v_max3_f32 v50, v66, v104, v105
	v_max3_f32 v50, v50, v106, v107
	s_waitcnt lgkmcnt(4)
	v_mfma_f32_32x32x16_bf16 v[2:17], v[54:57], v[214:217], v[2:17]
	v_max3_f32 v50, v50, v108, v109
	v_max3_f32 v50, v50, v110, v111
	v_max3_f32 v50, v50, v112, v113
	v_max3_f32 v50, v50, v82, v83
	v_max3_f32 v50, v50, v84, v85
	v_max3_f32 v50, v50, v86, v87
	v_max3_f32 v50, v50, v88, v89
	s_waitcnt lgkmcnt(2)
	v_mfma_f32_32x32x16_bf16 v[2:17], v[58:61], v[218:221], v[2:17]
	v_max3_f32 v50, v50, v90, v91
	v_max3_f32 v50, v50, v92, v93
	v_max3_f32 v50, v50, v94, v95
	v_max3_f32 v50, v50, v96, v97
	v_mov_b32_e32 v51, v50
	s_nop 1
	v_permlane32_swap_b32_e32 v50, v51
	s_waitcnt lgkmcnt(0)
	v_mfma_f32_32x32x16_bf16 v[2:17], v[62:65], v[222:225], v[2:17]
	v_max_f32_e32 v51, v51, v51
	v_max_f32_e32 v50, v50, v50
	v_max_f32_e32 v126, v50, v51
	v_cmp_ge_f32_e32 vcc, s80, v126
	s_cmp_lg_u64 vcc, exec
	s_cselect_b64 s[6:7], -1, 0
	s_mov_b64 s[16:17], -1
	s_mov_b64 vcc, s[6:7]
	s_cbranch_vccnz .LBB0_2269
	s_andn2_b64 vcc, exec, s[16:17]
	s_cbranch_vccz .LBB0_2270

; template <bool FIRST> DEVI bool partialSM(f32x16& p0, f32x16& p1, float& m_reg, float& alpha) {
;     float pmax = p0[0];
; #pragma unroll
;     for (int r = 1; r < 16; ++r) pmax = fmaxf(pmax, p0[r]);
; #pragma unroll
;     for (int r = 0; r < 16; ++r) pmax = fmaxf(pmax, p1[r]);
;     { auto rr = __builtin_amdgcn_permlane32_swap(__float_as_uint(pmax), __float_as_uint(pmax), false, false);
;       pmax = fmaxf(__uint_as_float(rr[0]), __uint_as_float(rr[1])); }
;     if (FIRST) { m_reg = pmax; alpha = 1.f;
; #pragma unroll
;         for (int r = 0; r < 16; ++r) { p0[r] = __builtin_amdgcn_exp2f(p0[r] - pmax); p1[r] = p1[r] - pmax; }
;         return false;
;     } else if (__builtin_expect(__all(pmax <= ATT_THR), 1)) { alpha = 1.f;
; #pragma unroll
;         for (int r = 0; r < 16; ++r) p0[r] = __builtin_amdgcn_exp2f(p0[r]);
;         return false;
;     } else { const float d = fmaxf(pmax, 0.f); alpha = __builtin_amdgcn_exp2f(-d); m_reg += d;
; #pragma unroll
;         for (int r = 0; r < 16; ++r) { p0[r] = __builtin_amdgcn_exp2f(p0[r] - d); p1[r] = p1[r] - d; }
;         return true;
;     }
; }
; DEVI void finishSM(f32x16& p0, f32x16& p1, float alpha, float& l_reg, bf16x8& pa0, bf16x8& pa1, bf16x8& pa2, bf16x8& pa3) {
; #pragma unroll
;     for (int r = 0; r < 16; ++r) p1[r] = __builtin_amdgcn_exp2f(p1[r]);
;     f32x2 s2 = (f32x2){p0[0], p0[1]} + (f32x2){p1[0], p1[1]};
; #pragma unroll
;     for (int r = 2; r < 16; r += 2) s2 += (f32x2){p0[r], p0[r + 1]} + (f32x2){p1[r], p1[r + 1]};
;     float ps = s2[0] + s2[1];
;     { auto rr = __builtin_amdgcn_permlane32_swap(__float_as_uint(ps), __float_as_uint(ps), false, false);
;       ps = __uint_as_float(rr[0]) + __uint_as_float(rr[1]); }
;     l_reg = l_reg * alpha + ps;
;     ...
;     PK4(p0, 0, pa0); PK4(p0, 8, pa1); PK4(p1, 0, pa2); PK4(p1, 8, pa3);
;     ...
; }
; DEVI void qkt(f32x16& p0, f32x16& p1, const char* Kb, const bf16x8 (&qr)[6], int r32, int hi, const f32x16& cinit) {
; #pragma unroll
; DEVI void attn_unit8(const Params& p, char* smem, int unit, int l, int& cvs  , CvRun& crun) {
;     ...
;         if (T + 2 < NTILE) B_DMA(T + 2, s2);
;         qkt(pA0, pA1, K_lds + s1 * 24576, qr, r32, hi, cinit);
;         finishSM(pB0, pB1, alB, l_reg, pa0, pa1, pa2, pa3);
;         pv_both(o[0], o[1], vb + 8192, pa0, pa1, pa2, pa3);
;         { const bool rr_ = partialSM<false>(pA0, pA1, m_reg, alA); B_RESC(alA, rr_); }
.LBB0_2266:
	s_mul_i32 s6, s61, 0x6000
	s_add_i32 s6, s96, s6
	v_lshl_add_u64 v[82:83], v[118:119], 0, s[12:13]
	s_mov_b32 m0, s6
	s_barrier
	global_load_lds_dwordx4 v[82:83], off
	v_lshl_add_u64 v[82:83], v[120:121], 0, s[12:13]
	s_add_i32 m0, s6, 0x2000
	v_exp_f32_e32 v66, v66
	global_load_lds_dwordx4 v[82:83], off
	s_add_i32 m0, s6, 0x4000
	s_lshl_b32 s6, s61, 14
	v_lshl_add_u64 v[82:83], v[122:123], 0, s[12:13]
	s_add_i32 s6, s97, s6
	global_load_lds_dwordx4 v[82:83], off
	s_mov_b32 m0, s6
	v_lshl_add_u64 v[82:83], v[116:117], 0, s[40:41]
	global_load_lds_dwordx4 v[116:117], off
	s_add_i32 m0, s6, 0x2000
	s_mul_i32 s6, s2, 0x6000
	global_load_lds_dwordx4 v[82:83], off
	s_add_i32 s6, s6, 0
	v_add_u32_e32 v86, s6, v129
	ds_read_b128 v[82:85], v86
	ds_read_b128 v[212:215], v86 offset:6144
	s_waitcnt lgkmcnt(1)
	v_mfma_f32_32x32x16_bf16 v[98:113], v[82:85], v[150:153], v[34:49]
	v_add_u32_e32 v126, s6, v184
	v_exp_f32_e32 v67, v67
	v_exp_f32_e32 v68, v68
	v_exp_f32_e32 v69, v69
	v_exp_f32_e32 v70, v70
	v_exp_f32_e32 v71, v71
	v_exp_f32_e32 v72, v72
	s_waitcnt lgkmcnt(0)
	v_mfma_f32_32x32x16_bf16 v[82:97], v[212:215], v[150:153], v[34:49]
	ds_read_b128 v[212:215], v126
	ds_read_b128 v[216:219], v126 offset:6144
	v_add_u32_e32 v126, s6, v185
	v_exp_f32_e32 v73, v73
	v_exp_f32_e32 v74, v74
	v_exp_f32_e32 v75, v75
	v_exp_f32_e32 v76, v76
	v_exp_f32_e32 v77, v77
	s_waitcnt lgkmcnt(1)
	v_mfma_f32_32x32x16_bf16 v[98:113], v[212:215], v[138:141], v[98:113]
	v_exp_f32_e32 v78, v78
	v_exp_f32_e32 v79, v79
	v_exp_f32_e32 v80, v80
	v_exp_f32_e32 v81, v81
	v_add_u32_e32 v174, 0x2000, v203
	s_waitcnt lgkmcnt(0)
	v_mfma_f32_32x32x16_bf16 v[82:97], v[216:219], v[138:141], v[82:97]
	ds_read_b128 v[212:215], v126
	ds_read_b128 v[216:219], v126 offset:6144
	v_add_u32_e32 v126, s6, v205
	s_waitcnt lgkmcnt(1)
	v_mfma_f32_32x32x16_bf16 v[98:113], v[212:215], v[134:137], v[98:113]
	ds_read_b128 v[212:215], v126
	ds_read_b128 v[220:223], v126 offset:6144
	v_add_u32_e32 v126, s6, v206
	s_waitcnt lgkmcnt(2)
	v_mfma_f32_32x32x16_bf16 v[82:97], v[216:219], v[134:137], v[82:97]
	ds_read_b128 v[216:219], v126
	ds_read_b128 v[224:227], v126 offset:6144
	v_add_u32_e32 v126, s6, v207
	ds_read_b128 v[228:231], v126
	ds_read_b128 v[232:235], v126 offset:6144
	v_pk_add_f32 v[126:127], v[50:51], v[66:67]
	v_cvt_pk_bf16_f32 v50, v50, v51
	v_cvt_pk_bf16_f32 v51, v52, v53
	s_waitcnt lgkmcnt(5)
	v_mfma_f32_32x32x16_bf16 v[98:113], v[212:215], v[130:133], v[98:113]
	v_add_f32_e64 v212, v52, v68
	v_add_f32_e64 v213, v53, v69
	v_cvt_pk_bf16_f32 v52, v54, v55
	v_cvt_pk_bf16_f32 v53, v56, v57
	v_add_f32_e64 v126, v212, v126
	v_add_f32_e64 v127, v213, v127
	v_add_f32_e64 v212, v54, v70
	v_add_f32_e64 v213, v55, v71
	v_cvt_pk_bf16_f32 v54, v58, v59
	s_waitcnt lgkmcnt(4)
	v_mfma_f32_32x32x16_bf16 v[82:97], v[220:223], v[130:133], v[82:97]
	v_add_f32_e64 v126, v212, v126
	v_add_f32_e64 v127, v213, v127
	v_add_f32_e64 v212, v56, v72
	v_add_f32_e64 v213, v57, v73
	v_cvt_pk_bf16_f32 v55, v60, v61
	v_cvt_pk_bf16_f32 v56, v62, v63
	v_cvt_pk_bf16_f32 v57, v64, v65
	v_add_f32_e64 v126, v212, v126
	v_add_f32_e64 v127, v213, v127
	v_pk_add_f32 v[212:213], v[58:59], v[74:75]
	v_cvt_pk_bf16_f32 v58, v66, v67
	v_cvt_pk_bf16_f32 v59, v68, v69
	s_waitcnt lgkmcnt(3)
	v_mfma_f32_32x32x16_bf16 v[98:113], v[216:219], v[146:149], v[98:113]
	v_add_f32_e64 v126, v212, v126
	v_add_f32_e64 v127, v213, v127
	v_add_f32_e64 v212, v60, v76
	v_add_f32_e64 v213, v61, v77
	v_cvt_pk_bf16_f32 v60, v70, v71
	v_cvt_pk_bf16_f32 v61, v72, v73
	v_add_f32_e64 v126, v212, v126
	v_add_f32_e64 v127, v213, v127
	v_pk_add_f32 v[212:213], v[62:63], v[78:79]
	v_cvt_pk_bf16_f32 v62, v74, v75
	v_cvt_pk_bf16_f32 v63, v76, v77
	s_waitcnt lgkmcnt(2)
	v_mfma_f32_32x32x16_bf16 v[82:97], v[224:227], v[146:149], v[82:97]
	v_add_f32_e64 v126, v212, v126
	v_add_f32_e64 v127, v213, v127
	v_add_f32_e64 v212, v64, v80
	v_add_f32_e64 v213, v65, v81
	v_cvt_pk_bf16_f32 v64, v78, v79
	v_cvt_pk_bf16_f32 v65, v80, v81
	ds_read_b64_tr_b16 v[66:67], v174 offset:0
	ds_read_b64_tr_b16 v[68:69], v174 offset:0x400
	ds_read_b64_tr_b16 v[70:71], v174 offset:0x800
	ds_read_b64_tr_b16 v[72:73], v174 offset:0xc00
	ds_read_b64_tr_b16 v[74:75], v174 offset:0x1000
	ds_read_b64_tr_b16 v[76:77], v174 offset:0x1400
	ds_read_b64_tr_b16 v[78:79], v174 offset:0x1800
	ds_read_b64_tr_b16 v[80:81], v174 offset:0x1c00
	v_add_f32_e64 v126, v212, v126
	v_add_f32_e64 v127, v213, v127
	ds_read_b64_tr_b16 v[212:213], v174 offset:0x200
	ds_read_b64_tr_b16 v[214:215], v174 offset:0x600
	ds_read_b64_tr_b16 v[216:217], v174 offset:0xa00
	s_waitcnt lgkmcnt(12)
	v_mfma_f32_32x32x16_bf16 v[98:113], v[228:231], v[142:145], v[98:113]
	ds_read_b64_tr_b16 v[218:219], v174 offset:0xe00
	ds_read_b64_tr_b16 v[220:221], v174 offset:0x1200
	ds_read_b64_tr_b16 v[222:223], v174 offset:0x1600
	ds_read_b64_tr_b16 v[224:225], v174 offset:0x1a00
	ds_read_b64_tr_b16 v[226:227], v174 offset:0x1e00
	v_pk_add_f32 v[126:127], v[126:127], v[126:127] op_sel:[0,1] op_sel_hi:[1,0]
	s_waitcnt lgkmcnt(15)
	v_mfma_f32_32x32x16_bf16 v[82:97], v[232:235], v[142:145], v[82:97]
	v_mov_b32_e32 v127, v126
	s_nop 1
	v_permlane32_swap_b32_e32 v126, v127
	s_waitcnt lgkmcnt(14)
	v_mfma_f32_32x32x16_bf16 v[18:33], v[50:53], v[66:69], v[18:33]
	s_waitcnt lgkmcnt(12)
	v_mfma_f32_32x32x16_bf16 v[18:33], v[54:57], v[70:73], v[18:33]
	s_waitcnt lgkmcnt(10)
	v_mfma_f32_32x32x16_bf16 v[18:33], v[58:61], v[74:77], v[18:33]
	s_waitcnt lgkmcnt(8)
	v_mfma_f32_32x32x16_bf16 v[18:33], v[62:65], v[78:81], v[18:33]
	s_waitcnt lgkmcnt(6)
	v_mfma_f32_32x32x16_bf16 v[2:17], v[50:53], v[212:215], v[2:17]
	s_nop 0
	v_max_f32_e32 v66, v99, v99
	v_max_f32_e32 v67, v98, v98
	v_max_f32_e32 v66, v67, v66
	v_max3_f32 v66, v66, v100, v101
	v_max3_f32 v66, v66, v102, v103
	v_max3_f32 v50, v66, v104, v105
	v_max3_f32 v50, v50, v106, v107
	s_waitcnt lgkmcnt(4)
	v_mfma_f32_32x32x16_bf16 v[2:17], v[54:57], v[216:219], v[2:17]
	v_max3_f32 v50, v50, v108, v109
	v_max3_f32 v50, v50, v110, v111
	v_max3_f32 v50, v50, v112, v113
	v_max3_f32 v50, v50, v82, v83
	v_max3_f32 v50, v50, v84, v85
	v_max3_f32 v50, v50, v86, v87
	v_max3_f32 v50, v50, v88, v89
	s_waitcnt lgkmcnt(2)
	v_mfma_f32_32x32x16_bf16 v[2:17], v[58:61], v[220:223], v[2:17]
	v_max3_f32 v50, v50, v90, v91
	v_max3_f32 v50, v50, v92, v93
	v_max3_f32 v50, v50, v94, v95
	v_max3_f32 v50, v50, v96, v97
	v_mov_b32_e32 v51, v50
	s_nop 1
	v_permlane32_swap_b32_e32 v50, v51
	s_waitcnt lgkmcnt(0)
	v_mfma_f32_32x32x16_bf16 v[2:17], v[62:65], v[224:227], v[2:17]
	v_max_f32_e32 v51, v51, v51
	v_max_f32_e32 v50, v50, v50
	v_max_f32_e32 v174, v50, v51
	v_cmp_ge_f32_e32 vcc, s80, v174
	s_cmp_lg_u64 vcc, exec
	s_cselect_b64 s[6:7], -1, 0
	s_mov_b64 s[14:15], -1
	s_mov_b64 vcc, s[6:7]
	s_cbranch_vccnz .LBB0_2275
	s_andn2_b64 vcc, exec, s[14:15]
	s_cbranch_vccz .LBB0_2276

; DEVI unsigned xb_add(unsigned* p, unsigned v) { return __hip_atomic_fetch_add(p, v, __ATOMIC_RELAXED, __HIP_MEMORY_SCOPE_AGENT); }
; DEVI void xcd_barrier(const XcdBarrier& b) {
;     asm volatile("s_waitcnt vmcnt(0)" ::: "memory");
;     __syncthreads();
;     if (threadIdx.x == 0) {
;         unsigned* bar = b.bar;
;         __builtin_amdgcn_s_waitcnt(0);
;         unsigned nloc = b.st[0], nx = b.st[1];
;         if (nloc == 0u) { xcd_barrier_complete(bar, b.x, nloc, nx); b.st[0] = nloc; b.st[1] = nx; }
;         const unsigned old = xb_add(&bar[XB_XSUB(b.x)], 1u);
.LBB0_2374:
	s_setprio 0
	s_mov_b64 s[6:7], s[0:1]
	s_getreg_b32 s2, hwreg(HW_REG_XCC_ID, 0, 4)
	s_waitcnt vmcnt(0)
	s_barrier
	s_mov_b64 s[4:5], exec
	v_readlane_b32 s8, v248, 0
	v_readlane_b32 s9, v248, 1
	s_and_b64 s[8:9], s[4:5], s[8:9]
	s_mov_b64 exec, s[8:9]
	s_cbranch_execz .LBB0_2426
	s_add_i32 s8, 0, 0x258f0
	v_mov_b32_e32 v2, s8
	s_load_dwordx2 s[6:7], s[6:7], 0xf8
	s_waitcnt vmcnt(0) expcnt(0) lgkmcnt(0)
	ds_read_b32 v4, v2
	s_add_i32 s8, 0, 0x258f4
	v_mov_b32_e32 v2, s8
	ds_read_b32 v2, v2
	s_and_b32 s2, s2, 15
	s_waitcnt lgkmcnt(1)
	v_cmp_ne_u32_e32 vcc, 0, v4
	s_cbranch_vccnz .LBB0_2390
	v_readlane_b32 s8, v248, 2
	v_readlane_b32 s9, v248, 3
	s_load_dwordx2 s[12:13], s[8:9], 0x4
	s_add_u32 s8, s6, 0x1000
	s_addc_u32 s9, s7, 0
	s_add_u32 s10, s6, 0x1100
	s_addc_u32 s11, s7, 0
	s_waitcnt lgkmcnt(0)
	s_mul_i32 s22, s12, s33
	s_add_u32 s12, s6, 0x1200
	s_mul_i32 s22, s22, s13
	s_addc_u32 s13, s7, 0
	s_add_u32 s14, s6, 0x1300
	s_addc_u32 s15, s7, 0
	s_mov_b32 s23, 1
	v_mov_b32_e32 v18, 0
	s_branch .LBB0_2378

; DEVI void phase_combine(const Params& p, char* smem, int l) {
;     ...
;     for (int t = gw; t < T_; t += nw) {
;         const int b = t >> 12;
;         const size_t slot = slot_nx;
;         { const int tn = t + nw; slot_nx = (size_t)T_ * 8 + tn;
;           if (lane < 8 && tn < T_) slot_nx = (size_t)mt.rstart[tke[tn * 8 + lane]] + tkp[tn * 8 + lane]; }
;         u32x4 w[9];
; #pragma unroll
;         for (int k = 0; k < 9; ++k) { const size_t sl = (size_t)(unsigned)__builtin_amdgcn_readlane((int)(unsigned)slot, k);
;             w[k] = *(const u32x4*)(ysl + sl * 1024 + lane * 16); }
;         const u32x4 xr0 = *(const u32x4*)(xab + (size_t)t * 1024 + lane * 16), xr1 = *(const u32x4*)(xab + (size_t)t * 1024 + lane * 16 + 8);
.LBB0_3296:
	v_add_u32_e32 v104, s86, v105
	v_cmp_gt_i32_e64 s[4:5], s29, v104
	v_add_u32_e32 v97, 0x40000, v104
	v_cmp_lt_i32_e32 vcc, s28, v104
	s_and_b64 s[6:7], s[2:3], s[4:5]
	s_and_b64 s[4:5], exec, vcc
	s_or_b64 s[14:15], s[4:5], s[14:15]
	v_readlane_b32 s12, v48, 0
	s_lshl_b64 s[4:5], s[12:13], 10
	v_readlane_b32 s12, v48, 1
	v_lshl_add_u64 v[50:51], v[94:95], 0, s[4:5]
	s_lshl_b64 s[4:5], s[12:13], 10
	v_readlane_b32 s12, v48, 2
	v_lshl_add_u64 v[52:53], v[94:95], 0, s[4:5]
	s_lshl_b64 s[4:5], s[12:13], 10
	v_readlane_b32 s12, v48, 3
	flat_load_dwordx4 v[88:91], v[50:51]
	flat_load_dwordx4 v[80:83], v[52:53]
	v_lshl_add_u64 v[50:51], v[94:95], 0, s[4:5]
	s_lshl_b64 s[4:5], s[12:13], 10
	v_readlane_b32 s12, v48, 4
	v_lshl_add_u64 v[52:53], v[94:95], 0, s[4:5]
	s_lshl_b64 s[4:5], s[12:13], 10
	v_readlane_b32 s12, v48, 5
	flat_load_dwordx4 v[84:87], v[50:51]
	flat_load_dwordx4 v[72:75], v[52:53]
	v_lshl_add_u64 v[50:51], v[94:95], 0, s[4:5]
	s_lshl_b64 s[4:5], s[12:13], 10
	v_readlane_b32 s12, v48, 6
	v_lshl_add_u64 v[52:53], v[94:95], 0, s[4:5]
	s_lshl_b64 s[4:5], s[12:13], 10
	v_readlane_b32 s12, v48, 7
	flat_load_dwordx4 v[76:79], v[50:51]
	flat_load_dwordx4 v[64:67], v[52:53]
	v_lshl_add_u64 v[50:51], v[94:95], 0, s[4:5]
	s_lshl_b64 s[4:5], s[12:13], 10
	v_readlane_b32 s12, v48, 8
	v_lshl_add_u64 v[52:53], v[94:95], 0, s[4:5]
	s_lshl_b64 s[4:5], s[12:13], 10
	v_lshl_add_u64 v[106:107], v[94:95], 0, s[4:5]
	flat_load_dwordx4 v[68:71], v[50:51]
	flat_load_dwordx4 v[60:63], v[52:53]
	flat_load_dwordx4 v[56:59], v[106:107]
	s_nop 0
	flat_load_dwordx4 v[52:55], v[100:101]
	flat_load_dwordx4 v[48:51], v[100:101] offset:16
	s_and_saveexec_b64 s[4:5], s[6:7]
	s_cbranch_execz .Lmy_cmb_skip_b
	v_ashrrev_i32_e32 v97, 31, v96
	v_lshlrev_b64 v[250:251], 2, v[96:97]
	v_lshl_add_u64 v[252:253], s[8:9], 0, v[250:251]
	flat_load_dword v254, v[252:253]
	v_lshl_add_u64 v[250:251], s[10:11], 0, v[250:251]
	flat_load_dword v255, v[250:251]
	s_waitcnt vmcnt(0) lgkmcnt(0)
	v_lshl_add_u32 v254, v254, 2, s19
	ds_read_b32 v254, v254 offset:61440
	s_waitcnt lgkmcnt(0)
	v_add_u32_e32 v97, v255, v254
.Lmy_cmb_skip_b:
	s_or_b64 exec, exec, s[4:5]
	v_ashrrev_i32_e32 v105, 12, v105
	v_cmp_ne_u32_e32 vcc, v105, v103
	s_and_saveexec_b64 s[4:5], vcc
	s_cbranch_execz .LBB0_3295
	s_load_dwordx2 s[6:7], s[0:1], 0x108
	v_add_u32_e32 v32, 8, v105
	v_mul_hi_i32_i24_e32 v33, 0x6000, v32
	v_mul_i32_i24_e32 v32, 0x6000, v32
	v_mov_b32_e32 v103, v105
	s_waitcnt lgkmcnt(0)
	v_lshl_add_u64 v[32:33], s[6:7], 0, v[32:33]
	v_lshl_add_u64 v[32:33], v[32:33], 0, v[92:93]
	v_add_co_u32_e32 v108, vcc, 0x5000, v32
	v_lshl_add_u64 v[106:107], v[32:33], 0, s[16:17]
	s_nop 0
	v_addc_co_u32_e32 v109, vcc, 0, v33, vcc
	global_load_dwordx4 v[32:35], v[108:109], off
	global_load_dwordx4 v[44:47], v[106:107], off offset:48
	global_load_dwordx4 v[40:43], v[106:107], off offset:32
	global_load_dwordx4 v[36:39], v[106:107], off offset:16
	s_branch .LBB0_3295

; #define LAS __attribute__((address_space(3)))
; #define PHASE(PH, L) do { run_phase<PH>(fresh_params(), smem, L); } while (0)
; #define GRID_BARRIER() do { XcdBarrier b_; b_.bar = fresh_params().bar; b_.x = xb_xcc_id(); b_.st = (volatile LAS unsigned*)(LAS char*)(smem + LDS_BYTES - 16); xcd_barrier(b_); } while (0)
; #define LAYER(l, LAST) do { PHASE_B(2, l); PHASE_B(3, l); PHASE_B(4, l); PHASE_B(5, l); PHASE_B(6, l); PHASE_B(7, l); PHASE_B(8, l); PHASE_B(9, l); PHASE(15, l); GRID_BARRIER(); PHASE_B(11, l); PHASE_B(12, l); \
;         PHASE(13, l); if (!(LAST)) GRID_BARRIER(); \
;         if (DUP_MASK & (1 << 13)) { GRID_BARRIER(); PHASE(13, l); GRID_BARRIER(); } } while (0)
; __global__ void __launch_bounds__(512, 2) k_mega(Params p_unused) {
;     extern __shared__ __attribute__((aligned(16))) char smem[];
;     { volatile LAS unsigned* xbw = (volatile LAS unsigned*)(LAS char*)(smem + LDS_BYTES - 16);
;       if (threadIdx.x == 0) { xbw[0] = 0u; xbw[1] = 0u; xbw[2] = 0u; xbw[3] = 0u; }
;       __syncthreads();
;       (void)xcd_barrier_post(fresh_params().bar, xbw); }
;     PHASE(0, 0); GRID_BARRIER(); if (DUP_MASK & 1) { PHASE(0, 0); GRID_BARRIER(); }
;     PHASE(1, 0); GRID_BARRIER(); if (DUP_MASK & 2) { PHASE(1, 0); GRID_BARRIER(); }
;     ...
;     LAYER(0, false);
;     LAYER(1, true);
; }
	.amdhsa_kernel _Z6k_mega6Params
		.amdhsa_group_segment_fixed_size 0
		.amdhsa_private_segment_fixed_size 0
		.amdhsa_kernarg_size 816
		.amdhsa_user_sgpr_count 2
		.amdhsa_user_sgpr_dispatch_ptr 0
		.amdhsa_user_sgpr_queue_ptr 0
		.amdhsa_user_sgpr_kernarg_segment_ptr 1
		.amdhsa_user_sgpr_dispatch_id 0
		.amdhsa_user_sgpr_kernarg_preload_length 0
		.amdhsa_user_sgpr_kernarg_preload_offset 0
		.amdhsa_user_sgpr_private_segment_size 0
		.amdhsa_uses_dynamic_stack 0
		.amdhsa_enable_private_segment 0
		.amdhsa_system_sgpr_workgroup_id_x 1
		.amdhsa_system_sgpr_workgroup_id_y 0
		.amdhsa_system_sgpr_workgroup_id_z 0
		.amdhsa_system_sgpr_workgroup_info 0
		.amdhsa_system_vgpr_workitem_id 0
		.amdhsa_next_free_vgpr 256
		.amdhsa_next_free_sgpr 100
		.amdhsa_accum_offset 256
		.amdhsa_reserve_vcc 1
		.amdhsa_float_round_mode_32 0
		.amdhsa_float_round_mode_16_64 0
		.amdhsa_float_denorm_mode_32 3
		.amdhsa_float_denorm_mode_16_64 3
		.amdhsa_dx10_clamp 1
		.amdhsa_ieee_mode 1
		.amdhsa_fp16_overflow 0
		.amdhsa_tg_split 0
		.amdhsa_exception_fp_ieee_invalid_op 0
		.amdhsa_exception_fp_denorm_src 0
		.amdhsa_exception_fp_ieee_div_zero 0
		.amdhsa_exception_fp_ieee_overflow 0
		.amdhsa_exception_fp_ieee_underflow 0
		.amdhsa_exception_fp_ieee_inexact 0
		.amdhsa_exception_int_div_zero 0
	.end_amdhsa_kernel

; #define LAS __attribute__((address_space(3)))
; #define PHASE(PH, L) do { run_phase<PH>(fresh_params(), smem, L); } while (0)
; #define GRID_BARRIER() do { XcdBarrier b_; b_.bar = fresh_params().bar; b_.x = xb_xcc_id(); b_.st = (volatile LAS unsigned*)(LAS char*)(smem + LDS_BYTES - 16); xcd_barrier(b_); } while (0)
; #define LAYER(l, LAST) do { PHASE_B(2, l); PHASE_B(3, l); PHASE_B(4, l); PHASE_B(5, l); PHASE_B(6, l); PHASE_B(7, l); PHASE_B(8, l); PHASE_B(9, l); PHASE(15, l); GRID_BARRIER(); PHASE_B(11, l); PHASE_B(12, l); \
;         PHASE(13, l); if (!(LAST)) GRID_BARRIER(); \
;         if (DUP_MASK & (1 << 13)) { GRID_BARRIER(); PHASE(13, l); GRID_BARRIER(); } } while (0)
; __global__ void __launch_bounds__(512, 2) k_mega(Params p_unused) {
;     extern __shared__ __attribute__((aligned(16))) char smem[];
;     { volatile LAS unsigned* xbw = (volatile LAS unsigned*)(LAS char*)(smem + LDS_BYTES - 16);
;       if (threadIdx.x == 0) { xbw[0] = 0u; xbw[1] = 0u; xbw[2] = 0u; xbw[3] = 0u; }
;       __syncthreads();
;       (void)xcd_barrier_post(fresh_params().bar, xbw); }
;     PHASE(0, 0); GRID_BARRIER(); if (DUP_MASK & 1) { PHASE(0, 0); GRID_BARRIER(); }
;     PHASE(1, 0); GRID_BARRIER(); if (DUP_MASK & 2) { PHASE(1, 0); GRID_BARRIER(); }
;     ...
;     LAYER(0, false);
;     LAYER(1, true);
; }
.Lfunc_end0:
	.size	_Z6k_mega6Params, .Lfunc_end0-_Z6k_mega6Params
	.set _Z6k_mega6Params.num_vgpr, 256
	.set _Z6k_mega6Params.num_agpr, 0
	.set _Z6k_mega6Params.numbered_sgpr, 100
	.set _Z6k_mega6Params.num_named_barrier, 0
	.set _Z6k_mega6Params.private_seg_size, 0
	.set _Z6k_mega6Params.uses_vcc, 1
	.set _Z6k_mega6Params.uses_flat_scratch, 0
	.set _Z6k_mega6Params.has_dyn_sized_stack, 0
	.set _Z6k_mega6Params.has_recursion, 0
	.set _Z6k_mega6Params.has_indirect_call, 0

; #define LAS __attribute__((address_space(3)))
; #define PHASE(PH, L) do { run_phase<PH>(fresh_params(), smem, L); } while (0)
; #define GRID_BARRIER() do { XcdBarrier b_; b_.bar = fresh_params().bar; b_.x = xb_xcc_id(); b_.st = (volatile LAS unsigned*)(LAS char*)(smem + LDS_BYTES - 16); xcd_barrier(b_); } while (0)
; #define LAYER(l, LAST) do { PHASE_B(2, l); PHASE_B(3, l); PHASE_B(4, l); PHASE_B(5, l); PHASE_B(6, l); PHASE_B(7, l); PHASE_B(8, l); PHASE_B(9, l); PHASE(15, l); GRID_BARRIER(); PHASE_B(11, l); PHASE_B(12, l); \
;         PHASE(13, l); if (!(LAST)) GRID_BARRIER(); \
;         if (DUP_MASK & (1 << 13)) { GRID_BARRIER(); PHASE(13, l); GRID_BARRIER(); } } while (0)
; __global__ void __launch_bounds__(512, 2) k_mega(Params p_unused) {
;     extern __shared__ __attribute__((aligned(16))) char smem[];
;     { volatile LAS unsigned* xbw = (volatile LAS unsigned*)(LAS char*)(smem + LDS_BYTES - 16);
;       if (threadIdx.x == 0) { xbw[0] = 0u; xbw[1] = 0u; xbw[2] = 0u; xbw[3] = 0u; }
;       __syncthreads();
;       (void)xcd_barrier_post(fresh_params().bar, xbw); }
;     PHASE(0, 0); GRID_BARRIER(); if (DUP_MASK & 1) { PHASE(0, 0); GRID_BARRIER(); }
;     PHASE(1, 0); GRID_BARRIER(); if (DUP_MASK & 2) { PHASE(1, 0); GRID_BARRIER(); }
;     ...
;     LAYER(0, false);
;     LAYER(1, true);
; }
amdhsa.kernels:
  - .agpr_count:     0
    .args:
      - .offset:         0
        .size:           560
        .value_kind:     by_value
      - .offset:         560
        .size:           4
        .value_kind:     hidden_block_count_x
      - .offset:         564
        .size:           4
        .value_kind:     hidden_block_count_y
      - .offset:         568
        .size:           4
        .value_kind:     hidden_block_count_z
      - .offset:         572
        .size:           2
        .value_kind:     hidden_group_size_x
      - .offset:         574
        .size:           2
        .value_kind:     hidden_group_size_y
      - .offset:         576
        .size:           2
        .value_kind:     hidden_group_size_z
      - .offset:         578
        .size:           2
        .value_kind:     hidden_remainder_x
      - .offset:         580
        .size:           2
        .value_kind:     hidden_remainder_y
      - .offset:         582
        .size:           2
        .value_kind:     hidden_remainder_z
      - .offset:         600
        .size:           8
        .value_kind:     hidden_global_offset_x
      - .offset:         608
        .size:           8
        .value_kind:     hidden_global_offset_y
      - .offset:         616
        .size:           8
        .value_kind:     hidden_global_offset_z
      - .offset:         624
        .size:           2
        .value_kind:     hidden_grid_dims
      - .offset:         680
        .size:           4
        .value_kind:     hidden_dynamic_lds_size
    .group_segment_fixed_size: 0
    .kernarg_segment_align: 8
    .kernarg_segment_size: 816
    .language:       OpenCL C
    .language_version:
      - 2
      - 0
    .max_flat_workgroup_size: 512
    .name:           _Z6k_mega6Params
    .private_segment_fixed_size: 0
    .sgpr_count:     106
    .sgpr_spill_count: 9
    .symbol:         _Z6k_mega6Params.kd
    .uniform_work_group_size: 1
    .uses_dynamic_stack: false
    .vgpr_count:     256
    .vgpr_spill_count: 0
    .wavefront_size: 64
